# P7 epilogue: VALU trimmed (903->721) AND stores widened (16 dword -> 4 dwordx4 per wave) together
# speedup vs baseline: 1.0157x; 1.0157x over previous
.LBB0_827:
	s_ashr_i32 s5, s4, 31
	s_lshl_b64 s[26:27], s[4:5], 14
	s_add_u32 s5, s82, s26
	s_addc_u32 s23, s83, s27
	s_ashr_i32 s11, s10, 31
	s_lshl_b64 s[26:27], s[10:11], 2
	s_add_u32 s5, s5, s26
	s_addc_u32 s11, s23, s27
	s_add_u32 s26, s5, s73
	s_addc_u32 s27, s11, 0
	global_load_dwordx4 v[8:11], v194, s[26:27]
	global_load_dwordx4 v[4:7], v194, s[26:27] offset:64
	v_mov_b32_e32 v195, v183
	v_lshl_add_u64 v[0:1], s[26:27], 0, v[194:195]
	s_movk_i32 s5, 0x2000
	v_add_co_u32_e32 v0, vcc, s5, v0
	v_mov_b32_e32 v18, v183
	s_nop 0
	v_addc_co_u32_e32 v1, vcc, 0, v1, vcc
	global_load_dwordx4 v[12:15], v[0:1], off
	s_nop 0
	global_load_dwordx4 v[0:3], v[0:1], off offset:64
	s_ashr_i32 s5, s45, 3
	s_ashr_i32 s11, s10, 7
	s_and_b32 s5, s5, -16
	s_add_i32 s26, s5, s11
	s_ashr_i32 s27, s26, 31
	s_lshl_b64 s[26:27], s[26:27], 14
	v_lshl_add_u64 v[16:17], v[188:189], 0, s[26:27]
	s_movk_i32 s5, 0x1000
	s_mov_b64 s[26:27], 0x40000
	v_bfe_u32 v251, v178, 4, 2
	v_mov_b32_e32 v255, 0
	v_mul_u32_u24_e32 v254, 0x7fc, v251
	v_lshl_add_u64 v[252:253], v[16:17], 0, v[254:255]
	v_lshl_add_u64 v[254:255], v[252:253], 0, s[26:27]
	s_waitcnt vmcnt(0)
	v_add_f32_e32 v12, 1.0, v12
	v_add_f32_e32 v13, 1.0, v13
	v_add_f32_e32 v14, 1.0, v14
	v_add_f32_e32 v15, 1.0, v15
	v_add_f32_e32 v0, 1.0, v0
	v_add_f32_e32 v1, 1.0, v1
	v_add_f32_e32 v2, 1.0, v2
	v_add_f32_e32 v3, 1.0, v3
	v_add_f32_e32 v19, v172, v8
	v_add_f32_e32 v20, v173, v9
	v_min_f32_e32 v19, 0x40e00000, v19
	v_min_f32_e32 v20, 0x40e00000, v20
	v_mul_f32_e32 v27, 0xc01d265f, v19
	v_mul_f32_e32 v29, 0xc01d265f, v20
	v_add_f32_e32 v21, v174, v10
	v_add_f32_e32 v22, v175, v11
	v_exp_f32_e32 v27, v27
	v_exp_f32_e32 v29, v29
	v_min_f32_e32 v21, 0x40e00000, v21
	v_min_f32_e32 v22, 0x40e00000, v22
	v_mul_f32_e32 v31, 0xc01d265f, v21
	v_mul_f32_e32 v33, 0xc01d265f, v22
	v_add_f32_e32 v23, v168, v4
	v_min_f32_e32 v23, 0x40e00000, v23
	v_exp_f32_e32 v31, v31
	v_exp_f32_e32 v33, v33
	v_add_f32_e32 v27, 1.0, v27
	v_add_f32_e32 v29, 1.0, v29
	v_mul_f32_e32 v35, 0xc01d265f, v23
	v_rcp_f32_e32 v27, v27
	v_rcp_f32_e32 v29, v29
	v_add_f32_e32 v26, v140, v12
	v_add_f32_e32 v28, v141, v13
	v_exp_f32_e32 v35, v35
	v_med3_f32 v26, v26, s80, v206
	v_med3_f32 v28, v28, s80, v206
	v_add_f32_e32 v31, 1.0, v31
	v_add_f32_e32 v33, 1.0, v33
	v_add_f32_e32 v25, v170, v6
	v_rcp_f32_e32 v31, v31
	v_rcp_f32_e32 v33, v33
	v_mul_f32_e32 v19, v19, v27
	v_mul_f32_e32 v20, v20, v29
	v_min_f32_e32 v25, 0x40e00000, v25
	v_mul_f32_e32 v19, v26, v19
	v_mul_f32_e32 v20, v28, v20
	v_add_f32_e32 v30, v142, v14
	v_add_f32_e32 v32, v143, v15
	v_mul_f32_e32 v38, 0xc01d265f, v25
	v_add_f32_e32 v35, 1.0, v35
	v_med3_f32 v30, v30, s80, v206
	v_med3_f32 v32, v32, s80, v206
	v_rcp_f32_e32 v35, v35
	v_cvt_pk_fp8_f32 v18, v19, v20
	v_add_f32_e32 v24, v169, v5
	v_exp_f32_e32 v38, v38
	v_mul_f32_e32 v21, v21, v31
	v_mul_f32_e32 v22, v22, v33
	v_min_f32_e32 v24, 0x40e00000, v24
	v_add_f32_e32 v34, v136, v0
	v_mul_f32_e32 v21, v30, v21
	v_mul_f32_e32 v22, v32, v22
	v_mul_f32_e32 v37, 0xc01d265f, v24
	v_med3_f32 v34, v34, s80, v206
	v_mov_b32_e32 v20, v21
	v_mov_b32_e32 v21, v22
	v_add_f32_e32 v22, v171, v7
	v_mul_f32_e32 v23, v23, v35
	v_cvt_pk_fp8_f32 v18, v20, v21 op_sel:[0,0,1]
	v_min_f32_e32 v22, 0x40e00000, v22
	v_exp_f32_e32 v37, v37
	v_mul_f32_e32 v19, v34, v23
	v_add_f32_e32 v21, 1.0, v38
	v_mul_f32_e32 v23, 0xc01d265f, v22
	v_rcp_f32_e32 v21, v21
	v_exp_f32_e32 v23, v23
	v_mov_b32_e32 v236, v18
	v_add_f32_e32 v18, v138, v2
	v_add_f32_e32 v37, 1.0, v37
	v_med3_f32 v18, v18, s80, v206
	v_rcp_f32_e32 v37, v37
	v_mul_f32_e32 v21, v25, v21
	v_mul_f32_e32 v18, v18, v21
	v_add_f32_e32 v21, 1.0, v23
	v_add_f32_e32 v36, v137, v1
	v_rcp_f32_e32 v21, v21
	v_med3_f32 v36, v36, s80, v206
	v_mul_f32_e32 v24, v24, v37
	v_mul_f32_e32 v20, v36, v24
	v_add_f32_e32 v23, v139, v3
	v_mul_f32_e32 v21, v22, v21
	v_mov_b32_e32 v22, v183
	v_cvt_pk_fp8_f32 v22, v19, v20
	v_med3_f32 v19, v23, s80, v206
	v_mul_f32_e32 v19, v19, v21
	v_cvt_pk_fp8_f32 v22, v18, v19 op_sel:[0,0,1]
	v_add_f32_e32 v18, v164, v8
	v_min_f32_e32 v18, 0x40e00000, v18
	v_mul_f32_e32 v19, 0xc01d265f, v18
	v_exp_f32_e32 v19, v19
	v_add_f32_e32 v21, v165, v9
	v_min_f32_e32 v21, 0x40e00000, v21
	v_mov_b32_e32 v240, v22
	v_add_f32_e32 v19, 1.0, v19
	v_mul_f32_e32 v22, 0xc01d265f, v21
	v_rcp_f32_e32 v19, v19
	v_exp_f32_e32 v22, v22
	v_add_f32_e32 v20, v132, v12
	v_mul_f32_e32 v18, v18, v19
	v_med3_f32 v19, v20, s80, v206
	v_mul_f32_e32 v18, v19, v18
	v_add_f32_e32 v19, 1.0, v22
	v_rcp_f32_e32 v19, v19
	v_add_f32_e32 v20, v133, v13
	v_med3_f32 v20, v20, s80, v206
	v_mul_f32_e32 v19, v21, v19
	v_mul_f32_e32 v19, v20, v19
	v_add_f32_e32 v20, v166, v10
	v_min_f32_e32 v20, 0x40e00000, v20
	v_mul_f32_e32 v21, 0xc01d265f, v20
	v_exp_f32_e32 v21, v21
	v_add_f32_e32 v23, v167, v11
	v_min_f32_e32 v23, 0x40e00000, v23
	v_mul_f32_e32 v24, 0xc01d265f, v23
	v_add_f32_e32 v21, 1.0, v21
	v_rcp_f32_e32 v21, v21
	v_exp_f32_e32 v24, v24
	v_add_f32_e32 v22, v134, v14
	v_mul_f32_e32 v20, v20, v21
	v_med3_f32 v21, v22, s80, v206
	v_mul_f32_e32 v20, v21, v20
	v_add_f32_e32 v21, 1.0, v24
	v_rcp_f32_e32 v21, v21
	v_add_f32_e32 v22, v135, v15
	v_mul_f32_e32 v21, v23, v21
	v_mov_b32_e32 v23, v183
	v_cvt_pk_fp8_f32 v23, v18, v19
	v_med3_f32 v18, v22, s80, v206
	v_mul_f32_e32 v18, v18, v21
	v_cvt_pk_fp8_f32 v23, v20, v18 op_sel:[0,0,1]
	v_add_f32_e32 v18, v160, v4
	v_min_f32_e32 v18, 0x40e00000, v18
	v_mul_f32_e32 v19, 0xc01d265f, v18
	v_exp_f32_e32 v19, v19
	v_add_f32_e32 v21, v161, v5
	v_min_f32_e32 v21, 0x40e00000, v21
	v_mul_f32_e32 v22, 0xc01d265f, v21
	v_add_f32_e32 v19, 1.0, v19
	v_rcp_f32_e32 v19, v19
	v_exp_f32_e32 v22, v22
	v_add_f32_e32 v20, v128, v0
	v_mul_f32_e32 v18, v18, v19
	v_med3_f32 v19, v20, s80, v206
	v_mul_f32_e32 v18, v19, v18
	v_add_f32_e32 v19, 1.0, v22
	v_rcp_f32_e32 v19, v19
	v_add_f32_e32 v20, v129, v1
	v_med3_f32 v20, v20, s80, v206
	v_mul_f32_e32 v19, v21, v19
	v_mul_f32_e32 v19, v20, v19
	v_add_f32_e32 v20, v162, v6
	v_min_f32_e32 v20, 0x40e00000, v20
	v_mul_f32_e32 v21, 0xc01d265f, v20
	v_exp_f32_e32 v21, v21
	v_mov_b32_e32 v237, v23
	v_add_f32_e32 v23, v163, v7
	v_min_f32_e32 v23, 0x40e00000, v23
	v_add_f32_e32 v21, 1.0, v21
	v_mul_f32_e32 v24, 0xc01d265f, v23
	v_rcp_f32_e32 v21, v21
	v_exp_f32_e32 v24, v24
	v_add_f32_e32 v22, v130, v2
	v_mul_f32_e32 v20, v20, v21
	v_med3_f32 v21, v22, s80, v206
	v_mul_f32_e32 v20, v21, v20
	v_add_f32_e32 v21, 1.0, v24
	v_rcp_f32_e32 v21, v21
	v_add_f32_e32 v22, v131, v3
	v_mul_f32_e32 v21, v23, v21
	v_mov_b32_e32 v23, v183
	v_cvt_pk_fp8_f32 v23, v18, v19
	v_med3_f32 v18, v22, s80, v206
	v_mul_f32_e32 v18, v18, v21
	v_cvt_pk_fp8_f32 v23, v20, v18 op_sel:[0,0,1]
	v_add_f32_e32 v18, v156, v8
	v_min_f32_e32 v18, 0x40e00000, v18
	v_mul_f32_e32 v19, 0xc01d265f, v18
	v_exp_f32_e32 v19, v19
	v_add_f32_e32 v21, v157, v9
	v_min_f32_e32 v21, 0x40e00000, v21
	v_mul_f32_e32 v22, 0xc01d265f, v21
	v_add_f32_e32 v19, 1.0, v19
	v_rcp_f32_e32 v19, v19
	v_exp_f32_e32 v22, v22
	v_add_f32_e32 v20, v124, v12
	v_mul_f32_e32 v18, v18, v19
	v_med3_f32 v19, v20, s80, v206
	v_mul_f32_e32 v18, v19, v18
	v_add_f32_e32 v19, 1.0, v22
	v_rcp_f32_e32 v19, v19
	v_add_f32_e32 v20, v125, v13
	v_med3_f32 v20, v20, s80, v206
	v_mul_f32_e32 v19, v21, v19
	v_mul_f32_e32 v19, v20, v19
	v_add_f32_e32 v20, v158, v10
	v_min_f32_e32 v20, 0x40e00000, v20
	v_mul_f32_e32 v21, 0xc01d265f, v20
	v_exp_f32_e32 v21, v21
	v_mov_b32_e32 v241, v23
	v_add_f32_e32 v23, v159, v11
	v_min_f32_e32 v23, 0x40e00000, v23
	v_add_f32_e32 v21, 1.0, v21
	v_mul_f32_e32 v24, 0xc01d265f, v23
	v_rcp_f32_e32 v21, v21
	v_exp_f32_e32 v24, v24
	v_add_f32_e32 v22, v126, v14
	v_mul_f32_e32 v20, v20, v21
	v_med3_f32 v21, v22, s80, v206
	v_mul_f32_e32 v20, v21, v20
	v_add_f32_e32 v21, 1.0, v24
	v_rcp_f32_e32 v21, v21
	v_add_f32_e32 v22, v127, v15
	v_mul_f32_e32 v21, v23, v21
	v_mov_b32_e32 v23, v183
	v_cvt_pk_fp8_f32 v23, v18, v19
	v_med3_f32 v18, v22, s80, v206
	v_mul_f32_e32 v18, v18, v21
	v_cvt_pk_fp8_f32 v23, v20, v18 op_sel:[0,0,1]
	v_add_f32_e32 v18, v152, v4
	v_min_f32_e32 v20, 0x40e00000, v18
	v_mul_f32_e32 v18, 0xc01d265f, v20
	v_exp_f32_e32 v21, v18
	v_add_f32_e32 v24, v153, v5
	v_min_f32_e32 v24, 0x40e00000, v24
	v_mul_f32_e32 v25, 0xc01d265f, v24
	v_add_f32_e32 v21, 1.0, v21
	v_rcp_f32_e32 v21, v21
	v_exp_f32_e32 v25, v25
	v_add_f32_e32 v22, v120, v0
	v_mul_f32_e32 v20, v20, v21
	v_med3_f32 v21, v22, s80, v206
	v_mul_f32_e32 v20, v21, v20
	v_add_f32_e32 v21, 1.0, v25
	v_rcp_f32_e32 v21, v21
	v_add_f32_e32 v22, v121, v1
	v_med3_f32 v22, v22, s80, v206
	v_mul_f32_e32 v21, v24, v21
	v_mul_f32_e32 v21, v22, v21
	v_add_f32_e32 v22, v154, v6
	v_min_f32_e32 v22, 0x40e00000, v22
	v_mul_f32_e32 v24, 0xc01d265f, v22
	v_exp_f32_e32 v24, v24
	v_add_f32_e32 v26, v155, v7
	v_min_f32_e32 v26, 0x40e00000, v26
	v_mul_f32_e32 v27, 0xc01d265f, v26
	v_add_f32_e32 v24, 1.0, v24
	v_rcp_f32_e32 v24, v24
	v_exp_f32_e32 v27, v27
	v_add_f32_e32 v25, v122, v2
	v_mul_f32_e32 v22, v22, v24
	v_med3_f32 v24, v25, s80, v206
	v_mul_f32_e32 v22, v24, v22
	v_add_f32_e32 v24, 1.0, v27
	v_rcp_f32_e32 v24, v24
	v_add_f32_e32 v25, v123, v3
	v_med3_f32 v25, v25, s80, v206
	v_mul_f32_e32 v24, v26, v24
	v_mul_f32_e32 v24, v25, v24
	v_mov_b32_e32 v25, v183
	v_cvt_pk_fp8_f32 v25, v20, v21
	v_add_f32_e32 v20, v148, v8
	v_min_f32_e32 v20, 0x40e00000, v20
	v_mul_f32_e32 v21, 0xc01d265f, v20
	v_exp_f32_e32 v21, v21
	v_cvt_pk_fp8_f32 v25, v22, v24 op_sel:[0,0,1]
	v_add_f32_e32 v24, v149, v9
	v_min_f32_e32 v24, 0x40e00000, v24
	v_add_f32_e32 v21, 1.0, v21
	v_mul_f32_e32 v26, 0xc01d265f, v24
	v_rcp_f32_e32 v21, v21
	v_exp_f32_e32 v26, v26
	v_add_f32_e32 v22, v116, v12
	v_mul_f32_e32 v20, v20, v21
	v_med3_f32 v21, v22, s80, v206
	v_mul_f32_e32 v20, v21, v20
	v_add_f32_e32 v21, 1.0, v26
	v_rcp_f32_e32 v21, v21
	v_add_f32_e32 v22, v117, v13
	v_med3_f32 v22, v22, s80, v206
	v_mul_f32_e32 v21, v24, v21
	v_mul_f32_e32 v21, v22, v21
	v_add_f32_e32 v22, v150, v10
	v_min_f32_e32 v22, 0x40e00000, v22
	v_mul_f32_e32 v24, 0xc01d265f, v22
	v_exp_f32_e32 v24, v24
	v_add_f32_e32 v27, v151, v11
	v_min_f32_e32 v27, 0x40e00000, v27
	v_mul_f32_e32 v28, 0xc01d265f, v27
	v_add_f32_e32 v24, 1.0, v24
	v_rcp_f32_e32 v24, v24
	v_exp_f32_e32 v28, v28
	v_add_f32_e32 v26, v118, v14
	v_mul_f32_e32 v22, v22, v24
	v_med3_f32 v24, v26, s80, v206
	v_mul_f32_e32 v22, v24, v22
	v_add_f32_e32 v24, 1.0, v28
	v_rcp_f32_e32 v24, v24
	v_add_f32_e32 v26, v119, v15
	v_med3_f32 v26, v26, s80, v206
	v_mul_f32_e32 v24, v27, v24
	v_mul_f32_e32 v24, v26, v24
	v_mov_b32_e32 v26, v183
	v_cvt_pk_fp8_f32 v26, v20, v21
	v_add_f32_e32 v20, v144, v4
	v_min_f32_e32 v20, 0x40e00000, v20
	v_mul_f32_e32 v21, 0xc01d265f, v20
	v_exp_f32_e32 v21, v21
	v_cvt_pk_fp8_f32 v26, v22, v24 op_sel:[0,0,1]
	v_add_f32_e32 v24, v145, v5
	v_min_f32_e32 v24, 0x40e00000, v24
	v_add_f32_e32 v21, 1.0, v21
	v_mul_f32_e32 v27, 0xc01d265f, v24
	v_rcp_f32_e32 v21, v21
	v_exp_f32_e32 v27, v27
	v_add_f32_e32 v22, v112, v0
	v_mul_f32_e32 v20, v20, v21
	v_med3_f32 v21, v22, s80, v206
	v_mul_f32_e32 v20, v21, v20
	v_add_f32_e32 v21, 1.0, v27
	v_rcp_f32_e32 v21, v21
	v_add_f32_e32 v22, v113, v1
	v_med3_f32 v22, v22, s80, v206
	v_mul_f32_e32 v21, v24, v21
	v_mul_f32_e32 v21, v22, v21
	v_add_f32_e32 v22, v146, v6
	v_min_f32_e32 v22, 0x40e00000, v22
	v_mul_f32_e32 v24, 0xc01d265f, v22
	v_exp_f32_e32 v24, v24
	v_add_f32_e32 v28, v147, v7
	v_min_f32_e32 v28, 0x40e00000, v28
	v_mul_f32_e32 v29, 0xc01d265f, v28
	v_add_f32_e32 v24, 1.0, v24
	v_rcp_f32_e32 v24, v24
	v_exp_f32_e32 v29, v29
	v_add_f32_e32 v27, v114, v2
	v_mul_f32_e32 v22, v22, v24
	v_med3_f32 v24, v27, s80, v206
	v_mul_f32_e32 v22, v24, v22
	v_add_f32_e32 v24, 1.0, v29
	v_rcp_f32_e32 v24, v24
	v_add_f32_e32 v27, v115, v3
	v_mul_f32_e32 v24, v28, v24
	v_mov_b32_e32 v28, v183
	v_cvt_pk_fp8_f32 v28, v20, v21
	v_med3_f32 v20, v27, s80, v206
	v_mul_f32_e32 v20, v20, v24
	v_add_co_u32_e32 v18, vcc, s5, v16
	v_addc_co_u32_e32 v19, vcc, 0, v17, vcc
	v_cvt_pk_fp8_f32 v28, v22, v20 op_sel:[0,0,1]
	v_mov_b32_e32 v238, v23
	v_mov_b32_e32 v242, v25
	v_mov_b32_e32 v239, v26
	v_mov_b32_e32 v243, v28
	s_nop 1
	v_permlane32_swap_b32_e32 v236, v238
	v_permlane32_swap_b32_e32 v237, v239
	v_permlane32_swap_b32_e32 v240, v242
	v_permlane32_swap_b32_e32 v241, v243
	s_nop 0
	v_permlane16_swap_b32_e32 v236, v237
	v_permlane16_swap_b32_e32 v238, v239
	v_permlane16_swap_b32_e32 v240, v241
	v_permlane16_swap_b32_e32 v242, v243
	global_store_dwordx4 v[252:253], v[236:239], off
	global_store_dwordx4 v[252:253], v[240:243], off offset:16
	v_add_f32_e32 v18, v108, v8
	v_min_f32_e32 v20, 0x40e00000, v18
	v_mul_f32_e32 v18, 0xc01d265f, v20
	v_exp_f32_e32 v21, v18
	v_add_f32_e32 v23, v109, v9
	v_min_f32_e32 v23, 0x40e00000, v23
	v_mul_f32_e32 v24, 0xc01d265f, v23
	v_add_f32_e32 v21, 1.0, v21
	v_rcp_f32_e32 v21, v21
	v_exp_f32_e32 v24, v24
	v_add_f32_e32 v22, v76, v12
	v_mul_f32_e32 v20, v20, v21
	v_med3_f32 v21, v22, s80, v206
	v_mul_f32_e32 v20, v21, v20
	v_add_f32_e32 v21, 1.0, v24
	v_rcp_f32_e32 v21, v21
	v_add_f32_e32 v22, v77, v13
	v_med3_f32 v22, v22, s80, v206
	v_mul_f32_e32 v21, v23, v21
	v_mul_f32_e32 v21, v22, v21
	v_add_f32_e32 v22, v110, v10
	v_min_f32_e32 v22, 0x40e00000, v22
	v_mul_f32_e32 v23, 0xc01d265f, v22
	v_exp_f32_e32 v23, v23
	v_add_f32_e32 v25, v111, v11
	v_min_f32_e32 v25, 0x40e00000, v25
	v_mul_f32_e32 v26, 0xc01d265f, v25
	v_add_f32_e32 v23, 1.0, v23
	v_rcp_f32_e32 v23, v23
	v_exp_f32_e32 v26, v26
	v_add_f32_e32 v24, v78, v14
	v_mul_f32_e32 v22, v22, v23
	v_med3_f32 v23, v24, s80, v206
	v_mul_f32_e32 v22, v23, v22
	v_add_f32_e32 v23, 1.0, v26
	v_rcp_f32_e32 v23, v23
	v_add_f32_e32 v24, v79, v15
	v_mul_f32_e32 v23, v25, v23
	v_mov_b32_e32 v25, v183
	v_cvt_pk_fp8_f32 v25, v20, v21
	v_med3_f32 v20, v24, s80, v206
	v_mul_f32_e32 v20, v20, v23
	v_cvt_pk_fp8_f32 v25, v22, v20 op_sel:[0,0,1]
	v_add_f32_e32 v20, v104, v4
	v_min_f32_e32 v20, 0x40e00000, v20
	v_mul_f32_e32 v21, 0xc01d265f, v20
	v_exp_f32_e32 v21, v21
	v_add_f32_e32 v23, v105, v5
	v_min_f32_e32 v23, 0x40e00000, v23
	v_mul_f32_e32 v24, 0xc01d265f, v23
	v_add_f32_e32 v21, 1.0, v21
	v_rcp_f32_e32 v21, v21
	v_exp_f32_e32 v24, v24
	v_add_f32_e32 v22, v72, v0
	v_mul_f32_e32 v20, v20, v21
	v_med3_f32 v21, v22, s80, v206
	v_mul_f32_e32 v20, v21, v20
	v_add_f32_e32 v21, 1.0, v24
	v_rcp_f32_e32 v21, v21
	v_add_f32_e32 v22, v73, v1
	v_med3_f32 v22, v22, s80, v206
	v_mul_f32_e32 v21, v23, v21
	v_mul_f32_e32 v21, v22, v21
	v_add_f32_e32 v22, v106, v6
	v_min_f32_e32 v22, 0x40e00000, v22
	v_mul_f32_e32 v23, 0xc01d265f, v22
	s_mov_b32 s5, 0x41000
	v_lshl_add_u64 v[18:19], v[16:17], 0, s[26:27]
	v_add_co_u32_e32 v16, vcc, s5, v16
	v_exp_f32_e32 v23, v23
	s_nop 0
	v_addc_co_u32_e32 v17, vcc, 0, v17, vcc
	v_mov_b32_e32 v244, v25
	v_add_f32_e32 v25, v107, v7
	v_min_f32_e32 v25, 0x40e00000, v25
	v_add_f32_e32 v23, 1.0, v23
	v_mul_f32_e32 v26, 0xc01d265f, v25
	v_rcp_f32_e32 v23, v23
	v_exp_f32_e32 v26, v26
	v_add_f32_e32 v24, v74, v2
	v_mul_f32_e32 v22, v22, v23
	v_med3_f32 v23, v24, s80, v206
	v_mul_f32_e32 v22, v23, v22
	v_add_f32_e32 v23, 1.0, v26
	v_rcp_f32_e32 v23, v23
	v_add_f32_e32 v24, v75, v3
	v_mul_f32_e32 v23, v25, v23
	v_mov_b32_e32 v25, v183
	v_cvt_pk_fp8_f32 v25, v20, v21
	v_med3_f32 v20, v24, s80, v206
	v_mul_f32_e32 v20, v20, v23
	v_cvt_pk_fp8_f32 v25, v22, v20 op_sel:[0,0,1]
	v_add_f32_e32 v20, v100, v8
	v_min_f32_e32 v20, 0x40e00000, v20
	v_mul_f32_e32 v21, 0xc01d265f, v20
	v_exp_f32_e32 v21, v21
	v_add_f32_e32 v23, v101, v9
	v_min_f32_e32 v23, 0x40e00000, v23
	v_mul_f32_e32 v24, 0xc01d265f, v23
	v_add_f32_e32 v21, 1.0, v21
	v_rcp_f32_e32 v21, v21
	v_exp_f32_e32 v24, v24
	v_add_f32_e32 v22, v68, v12
	v_mul_f32_e32 v20, v20, v21
	v_med3_f32 v21, v22, s80, v206
	v_mul_f32_e32 v20, v21, v20
	v_add_f32_e32 v21, 1.0, v24
	v_rcp_f32_e32 v21, v21
	v_add_f32_e32 v22, v69, v13
	v_med3_f32 v22, v22, s80, v206
	v_mul_f32_e32 v21, v23, v21
	v_mul_f32_e32 v21, v22, v21
	v_add_f32_e32 v22, v102, v10
	v_min_f32_e32 v22, 0x40e00000, v22
	v_mul_f32_e32 v23, 0xc01d265f, v22
	v_exp_f32_e32 v23, v23
	v_mov_b32_e32 v236, v25
	v_add_f32_e32 v25, v103, v11
	v_min_f32_e32 v25, 0x40e00000, v25
	v_add_f32_e32 v23, 1.0, v23
	v_mul_f32_e32 v26, 0xc01d265f, v25
	v_rcp_f32_e32 v23, v23
	v_exp_f32_e32 v26, v26
	v_add_f32_e32 v24, v70, v14
	v_mul_f32_e32 v22, v22, v23
	v_med3_f32 v23, v24, s80, v206
	v_mul_f32_e32 v22, v23, v22
	v_add_f32_e32 v23, 1.0, v26
	v_rcp_f32_e32 v23, v23
	v_add_f32_e32 v24, v71, v15
	v_mul_f32_e32 v23, v25, v23
	v_mov_b32_e32 v25, v183
	v_cvt_pk_fp8_f32 v25, v20, v21
	v_med3_f32 v20, v24, s80, v206
	v_mul_f32_e32 v20, v20, v23
	v_cvt_pk_fp8_f32 v25, v22, v20 op_sel:[0,0,1]
	v_add_f32_e32 v20, v96, v4
	v_min_f32_e32 v20, 0x40e00000, v20
	v_mul_f32_e32 v21, 0xc01d265f, v20
	v_exp_f32_e32 v21, v21
	v_add_f32_e32 v23, v97, v5
	v_min_f32_e32 v23, 0x40e00000, v23
	v_mul_f32_e32 v24, 0xc01d265f, v23
	v_add_f32_e32 v21, 1.0, v21
	v_rcp_f32_e32 v21, v21
	v_exp_f32_e32 v24, v24
	v_add_f32_e32 v22, v64, v0
	v_mul_f32_e32 v20, v20, v21
	v_med3_f32 v21, v22, s80, v206
	v_mul_f32_e32 v20, v21, v20
	v_add_f32_e32 v21, 1.0, v24
	v_rcp_f32_e32 v21, v21
	v_add_f32_e32 v22, v65, v1
	v_med3_f32 v22, v22, s80, v206
	v_mul_f32_e32 v21, v23, v21
	v_mul_f32_e32 v21, v22, v21
	v_add_f32_e32 v22, v98, v6
	v_min_f32_e32 v22, 0x40e00000, v22
	v_mul_f32_e32 v23, 0xc01d265f, v22
	v_exp_f32_e32 v23, v23
	v_mov_b32_e32 v245, v25
	v_add_f32_e32 v25, v99, v7
	v_min_f32_e32 v25, 0x40e00000, v25
	v_add_f32_e32 v23, 1.0, v23
	v_mul_f32_e32 v26, 0xc01d265f, v25
	v_rcp_f32_e32 v23, v23
	v_exp_f32_e32 v26, v26
	v_add_f32_e32 v24, v66, v2
	v_mul_f32_e32 v22, v22, v23
	v_med3_f32 v23, v24, s80, v206
	v_mul_f32_e32 v22, v23, v22
	v_add_f32_e32 v23, 1.0, v26
	v_rcp_f32_e32 v23, v23
	v_add_f32_e32 v24, v67, v3
	v_mul_f32_e32 v23, v25, v23
	v_mov_b32_e32 v25, v183
	v_cvt_pk_fp8_f32 v25, v20, v21
	v_med3_f32 v20, v24, s80, v206
	v_mul_f32_e32 v20, v20, v23
	v_cvt_pk_fp8_f32 v25, v22, v20 op_sel:[0,0,1]
	v_add_f32_e32 v20, v92, v8
	v_min_f32_e32 v20, 0x40e00000, v20
	v_mul_f32_e32 v21, 0xc01d265f, v20
	v_exp_f32_e32 v21, v21
	v_mov_b32_e32 v237, v25
	v_add_f32_e32 v18, v60, v12
	v_med3_f32 v18, v18, s80, v206
	v_add_f32_e32 v19, 1.0, v21
	v_add_f32_e32 v21, v93, v9
	v_min_f32_e32 v21, 0x40e00000, v21
	v_mul_f32_e32 v22, 0xc01d265f, v21
	v_rcp_f32_e32 v19, v19
	v_exp_f32_e32 v22, v22
	v_mul_f32_e32 v19, v20, v19
	v_mul_f32_e32 v18, v18, v19
	v_add_f32_e32 v19, 1.0, v22
	v_rcp_f32_e32 v19, v19
	v_add_f32_e32 v20, v61, v13
	v_med3_f32 v20, v20, s80, v206
	v_mul_f32_e32 v19, v21, v19
	v_mul_f32_e32 v19, v20, v19
	v_add_f32_e32 v20, v94, v10
	v_min_f32_e32 v20, 0x40e00000, v20
	v_mul_f32_e32 v21, 0xc01d265f, v20
	v_exp_f32_e32 v21, v21
	v_add_f32_e32 v23, v95, v11
	v_min_f32_e32 v23, 0x40e00000, v23
	v_mul_f32_e32 v24, 0xc01d265f, v23
	v_add_f32_e32 v21, 1.0, v21
	v_rcp_f32_e32 v21, v21
	v_exp_f32_e32 v24, v24
	v_add_f32_e32 v22, v62, v14
	v_mul_f32_e32 v20, v20, v21
	v_med3_f32 v21, v22, s80, v206
	v_mul_f32_e32 v20, v21, v20
	v_add_f32_e32 v21, 1.0, v24
	v_rcp_f32_e32 v21, v21
	v_add_f32_e32 v22, v63, v15
	v_mul_f32_e32 v21, v23, v21
	v_mov_b32_e32 v23, v183
	v_cvt_pk_fp8_f32 v23, v18, v19
	v_med3_f32 v18, v22, s80, v206
	v_mul_f32_e32 v18, v18, v21
	v_cvt_pk_fp8_f32 v23, v20, v18 op_sel:[0,0,1]
	v_add_f32_e32 v18, v88, v4
	v_min_f32_e32 v18, 0x40e00000, v18
	v_mul_f32_e32 v19, 0xc01d265f, v18
	v_exp_f32_e32 v19, v19
	v_add_f32_e32 v21, v89, v5
	v_min_f32_e32 v21, 0x40e00000, v21
	v_mul_f32_e32 v22, 0xc01d265f, v21
	v_add_f32_e32 v19, 1.0, v19
	v_rcp_f32_e32 v19, v19
	v_exp_f32_e32 v22, v22
	v_add_f32_e32 v20, v56, v0
	v_mul_f32_e32 v18, v18, v19
	v_med3_f32 v19, v20, s80, v206
	v_mul_f32_e32 v18, v19, v18
	v_add_f32_e32 v19, 1.0, v22
	v_rcp_f32_e32 v19, v19
	v_add_f32_e32 v20, v57, v1
	v_med3_f32 v20, v20, s80, v206
	v_mul_f32_e32 v19, v21, v19
	v_mul_f32_e32 v19, v20, v19
	v_add_f32_e32 v20, v90, v6
	v_min_f32_e32 v20, 0x40e00000, v20
	v_mul_f32_e32 v21, 0xc01d265f, v20
	v_exp_f32_e32 v21, v21
	v_mov_b32_e32 v246, v23
	v_add_f32_e32 v23, v91, v7
	v_min_f32_e32 v23, 0x40e00000, v23
	v_add_f32_e32 v21, 1.0, v21
	v_mul_f32_e32 v24, 0xc01d265f, v23
	v_rcp_f32_e32 v21, v21
	v_exp_f32_e32 v24, v24
	v_add_f32_e32 v22, v58, v2
	v_mul_f32_e32 v20, v20, v21
	v_med3_f32 v21, v22, s80, v206
	v_mul_f32_e32 v20, v21, v20
	v_add_f32_e32 v21, 1.0, v24
	v_rcp_f32_e32 v21, v21
	v_add_f32_e32 v22, v59, v3
	v_mul_f32_e32 v21, v23, v21
	v_mov_b32_e32 v23, v183
	v_cvt_pk_fp8_f32 v23, v18, v19
	v_med3_f32 v18, v22, s80, v206
	v_mul_f32_e32 v18, v18, v21
	v_add_f32_e32 v8, v84, v8
	v_min_f32_e32 v8, 0x40e00000, v8
	v_cvt_pk_fp8_f32 v23, v20, v18 op_sel:[0,0,1]
	v_mul_f32_e32 v18, 0xc01d265f, v8
	v_exp_f32_e32 v18, v18
	v_add_f32_e32 v9, v85, v9
	v_min_f32_e32 v9, 0x40e00000, v9
	v_mul_f32_e32 v19, 0xc01d265f, v9
	v_add_f32_e32 v18, 1.0, v18
	v_rcp_f32_e32 v18, v18
	v_exp_f32_e32 v19, v19
	v_add_f32_e32 v12, v52, v12
	v_med3_f32 v12, v12, s80, v206
	v_mul_f32_e32 v8, v8, v18
	v_mul_f32_e32 v8, v12, v8
	v_add_f32_e32 v12, 1.0, v19
	v_rcp_f32_e32 v12, v12
	v_add_f32_e32 v13, v53, v13
	v_add_f32_e32 v10, v86, v10
	v_mul_f32_e32 v9, v9, v12
	v_med3_f32 v12, v13, s80, v206
	v_min_f32_e32 v10, 0x40e00000, v10
	v_mul_f32_e32 v9, v12, v9
	v_mul_f32_e32 v12, 0xc01d265f, v10
	v_exp_f32_e32 v12, v12
	v_add_f32_e32 v11, v87, v11
	v_min_f32_e32 v11, 0x40e00000, v11
	v_add_f32_e32 v13, v54, v14
	v_add_f32_e32 v12, 1.0, v12
	v_mul_f32_e32 v14, 0xc01d265f, v11
	v_rcp_f32_e32 v12, v12
	v_exp_f32_e32 v14, v14
	v_mul_f32_e32 v10, v10, v12
	v_med3_f32 v12, v13, s80, v206
	v_mul_f32_e32 v10, v12, v10
	v_add_f32_e32 v12, 1.0, v14
	v_rcp_f32_e32 v12, v12
	v_add_f32_e32 v13, v55, v15
	v_mul_f32_e32 v11, v11, v12
	v_mov_b32_e32 v12, v183
	v_cvt_pk_fp8_f32 v12, v8, v9
	v_med3_f32 v8, v13, s80, v206
	v_mul_f32_e32 v8, v8, v11
	v_add_f32_e32 v4, v80, v4
	v_min_f32_e32 v4, 0x40e00000, v4
	v_cvt_pk_fp8_f32 v12, v10, v8 op_sel:[0,0,1]
	v_mul_f32_e32 v8, 0xc01d265f, v4
	v_exp_f32_e32 v8, v8
	v_add_f32_e32 v5, v81, v5
	v_min_f32_e32 v5, 0x40e00000, v5
	v_mul_f32_e32 v9, 0xc01d265f, v5
	v_add_f32_e32 v8, 1.0, v8
	v_rcp_f32_e32 v8, v8
	v_exp_f32_e32 v9, v9
	v_add_f32_e32 v0, v48, v0
	v_med3_f32 v0, v0, s80, v206
	v_mul_f32_e32 v4, v4, v8
	v_mul_f32_e32 v0, v0, v4
	v_add_f32_e32 v4, 1.0, v9
	v_rcp_f32_e32 v4, v4
	v_add_f32_e32 v1, v49, v1
	v_med3_f32 v1, v1, s80, v206
	v_mul_f32_e32 v4, v5, v4
	v_mul_f32_e32 v1, v1, v4
	v_add_f32_e32 v4, v82, v6
	v_min_f32_e32 v4, 0x40e00000, v4
	v_mul_f32_e32 v5, 0xc01d265f, v4
	v_exp_f32_e32 v5, v5
	v_add_f32_e32 v6, v83, v7
	v_min_f32_e32 v6, 0x40e00000, v6
	v_mul_f32_e32 v7, 0xc01d265f, v6
	v_add_f32_e32 v5, 1.0, v5
	v_rcp_f32_e32 v5, v5
	v_exp_f32_e32 v7, v7
	v_add_f32_e32 v2, v50, v2
	v_med3_f32 v2, v2, s80, v206
	v_mul_f32_e32 v4, v4, v5
	v_mul_f32_e32 v2, v2, v4
	v_add_f32_e32 v4, 1.0, v7
	v_rcp_f32_e32 v4, v4
	v_add_f32_e32 v3, v51, v3
	v_mov_b32_e32 v5, v183
	v_cvt_pk_fp8_f32 v5, v0, v1
	v_mul_f32_e32 v4, v6, v4
	v_med3_f32 v0, v3, s80, v206
	v_mul_f32_e32 v0, v0, v4
	v_cvt_pk_fp8_f32 v5, v2, v0 op_sel:[0,0,1]
	s_andn2_b64 vcc, exec, s[24:25]
	v_mov_b32_e32 v238, v23
	v_mov_b32_e32 v247, v12
	v_mov_b32_e32 v239, v5
	s_nop 1
	v_permlane32_swap_b32_e32 v244, v246
	v_permlane32_swap_b32_e32 v245, v247
	v_permlane32_swap_b32_e32 v236, v238
	v_permlane32_swap_b32_e32 v237, v239
	s_nop 0
	v_permlane16_swap_b32_e32 v244, v245
	v_permlane16_swap_b32_e32 v246, v247
	v_permlane16_swap_b32_e32 v236, v237
	v_permlane16_swap_b32_e32 v238, v239
	global_store_dwordx4 v[254:255], v[244:247], off
	global_store_dwordx4 v[254:255], v[236:239], off offset:16
	s_cbranch_vccnz .LBB0_784
	v_mov_b32_e32 v48, 0
	s_mov_b32 s71, s44
	s_mov_b32 s8, s22
	s_mov_b64 s[6:7], s[20:21]
	s_mov_b32 s4, s18
	s_mov_b32 s45, s72
	s_mov_b32 s10, s19
	s_mov_b32 s76, s52
	v_mov_b32_e32 v49, v48
	v_mov_b32_e32 v50, v48
	v_mov_b32_e32 v51, v48
	v_mov_b32_e32 v52, v48
	v_mov_b32_e32 v53, v48
	v_mov_b32_e32 v54, v48
	v_mov_b32_e32 v55, v48
	v_mov_b32_e32 v56, v48
	v_mov_b32_e32 v57, v48
	v_mov_b32_e32 v58, v48
	v_mov_b32_e32 v59, v48
	v_mov_b32_e32 v60, v48
	v_mov_b32_e32 v61, v48
	v_mov_b32_e32 v62, v48
	v_mov_b32_e32 v63, v48
	v_mov_b32_e32 v64, v48
	v_mov_b32_e32 v65, v48
	v_mov_b32_e32 v66, v48
	v_mov_b32_e32 v67, v48
	v_mov_b32_e32 v68, v48
	v_mov_b32_e32 v69, v48
	v_mov_b32_e32 v70, v48
	v_mov_b32_e32 v71, v48
	v_mov_b32_e32 v72, v48
	v_mov_b32_e32 v73, v48
	v_mov_b32_e32 v74, v48
	v_mov_b32_e32 v75, v48
	v_mov_b32_e32 v76, v48
	v_mov_b32_e32 v77, v48
	v_mov_b32_e32 v78, v48
	v_mov_b32_e32 v79, v48
	v_mov_b32_e32 v80, v48
	v_mov_b32_e32 v81, v48
	v_mov_b32_e32 v82, v48
	v_mov_b32_e32 v83, v48
	v_mov_b32_e32 v84, v48
	v_mov_b32_e32 v85, v48
	v_mov_b32_e32 v86, v48
	v_mov_b32_e32 v87, v48
	v_mov_b32_e32 v88, v48
	v_mov_b32_e32 v89, v48
	v_mov_b32_e32 v90, v48
	v_mov_b32_e32 v91, v48
	v_mov_b32_e32 v92, v48
	v_mov_b32_e32 v93, v48
	v_mov_b32_e32 v94, v48
	v_mov_b32_e32 v95, v48
	v_mov_b32_e32 v96, v48
	v_mov_b32_e32 v97, v48
	v_mov_b32_e32 v98, v48
	v_mov_b32_e32 v99, v48
	v_mov_b32_e32 v100, v48
	v_mov_b32_e32 v101, v48
	v_mov_b32_e32 v102, v48
	v_mov_b32_e32 v103, v48
	v_mov_b32_e32 v104, v48
	v_mov_b32_e32 v105, v48
	v_mov_b32_e32 v106, v48
	v_mov_b32_e32 v107, v48
	v_mov_b32_e32 v108, v48
	v_mov_b32_e32 v109, v48
	v_mov_b32_e32 v110, v48
	v_mov_b32_e32 v111, v48
	v_mov_b32_e32 v112, v48
	v_mov_b32_e32 v113, v48
	v_mov_b32_e32 v114, v48
	v_mov_b32_e32 v115, v48
	v_mov_b32_e32 v116, v48
	v_mov_b32_e32 v117, v48
	v_mov_b32_e32 v118, v48
	v_mov_b32_e32 v119, v48
	v_mov_b32_e32 v120, v48
	v_mov_b32_e32 v121, v48
	v_mov_b32_e32 v122, v48
	v_mov_b32_e32 v123, v48
	v_mov_b32_e32 v124, v48
	v_mov_b32_e32 v125, v48
	v_mov_b32_e32 v126, v48
	v_mov_b32_e32 v127, v48
	v_mov_b32_e32 v128, v48
	v_mov_b32_e32 v129, v48
	v_mov_b32_e32 v130, v48
	v_mov_b32_e32 v131, v48
	v_mov_b32_e32 v132, v48
	v_mov_b32_e32 v133, v48
	v_mov_b32_e32 v134, v48
	v_mov_b32_e32 v135, v48
	v_mov_b32_e32 v136, v48
	v_mov_b32_e32 v137, v48
	v_mov_b32_e32 v138, v48
	v_mov_b32_e32 v139, v48
	v_mov_b32_e32 v140, v48
	v_mov_b32_e32 v141, v48
	v_mov_b32_e32 v142, v48
	v_mov_b32_e32 v143, v48
	v_mov_b32_e32 v144, v48
	v_mov_b32_e32 v145, v48
	v_mov_b32_e32 v146, v48
	v_mov_b32_e32 v147, v48
	v_mov_b32_e32 v148, v48
	v_mov_b32_e32 v149, v48
	v_mov_b32_e32 v150, v48
	v_mov_b32_e32 v151, v48
	v_mov_b32_e32 v152, v48
	v_mov_b32_e32 v153, v48
	v_mov_b32_e32 v154, v48
	v_mov_b32_e32 v155, v48
	v_mov_b32_e32 v156, v48
	v_mov_b32_e32 v157, v48
	v_mov_b32_e32 v158, v48
	v_mov_b32_e32 v159, v48
	v_mov_b32_e32 v160, v48
	v_mov_b32_e32 v161, v48
	v_mov_b32_e32 v162, v48
	v_mov_b32_e32 v163, v48
	v_mov_b32_e32 v164, v48
	v_mov_b32_e32 v165, v48
	v_mov_b32_e32 v166, v48
	v_mov_b32_e32 v167, v48
	v_mov_b32_e32 v168, v48
	v_mov_b32_e32 v169, v48
	v_mov_b32_e32 v170, v48
	v_mov_b32_e32 v171, v48
	v_mov_b32_e32 v172, v48
	v_mov_b32_e32 v173, v48
	v_mov_b32_e32 v174, v48
	v_mov_b32_e32 v175, v48
	s_branch .LBB0_784
